# on the P10 bias-prefetch version: leading half's re-align barrier moved ~90 instructions deeper into the now wait-free P10 epilogue
# speedup vs baseline: 1.0033x; 1.0008x over previous
.LBB0_1443:
	s_mov_b32 s100, s85
	s_mov_b32 s101, 0
	s_lshl_b64 s[100:101], s[100:101], 19
	s_add_u32 s100, s100, s18
	s_addc_u32 s101, s101, s19
	s_lshl_b32 vcc_lo, s10, 8
	s_add_u32 s100, s100, vcc_lo
	s_addc_u32 s101, s101, 0
	s_ashr_i32 s41, s40, 31
	s_lshl_b64 s[40:41], s[40:41], 13
	v_lshl_or_b32 v20, s10, 8, v183
	s_add_u32 s40, s12, s40
	s_addc_u32 s41, s13, s41
	v_ashrrev_i32_e32 v21, 31, v20
	v_lshl_add_u64 v[2:3], v[20:21], 2, s[40:41]
	v_mov_b32_e32 v14, v238
	v_mov_b32_e32 v15, v239
	v_mov_b32_e32 v16, v240
	v_mov_b32_e32 v17, v241
	v_mov_b32_e32 v10, v242
	v_mov_b32_e32 v11, v243
	v_mov_b32_e32 v12, v244
	v_mov_b32_e32 v13, v245
	v_mov_b32_e32 v6, v246
	v_mov_b32_e32 v7, v247
	v_mov_b32_e32 v8, v248
	v_mov_b32_e32 v9, v249
	s_nop 0
	v_mov_b32_e32 v2, v250
	v_mov_b32_e32 v3, v251
	v_mov_b32_e32 v4, v252
	v_mov_b32_e32 v5, v253
	v_mov_b32_e32 v24, 0
	v_mov_b32_e32 v25, 0
	v_mov_b32_e32 v26, 0
	v_mov_b32_e32 v27, 0
	v_mov_b32_e32 v28, 0
	v_mov_b32_e32 v29, 0
	v_mov_b32_e32 v30, 0
	v_mov_b32_e32 v31, 0
	v_lshl_add_u32 v18, s85, 8, v1
	v_mov_b32_e32 v174, 0
	v_mov_b32_e32 v175, 0
	v_ashrrev_i32_e32 v19, 31, v18
	v_or_b32_e32 v22, 16, v18
	v_or_b32_e32 v176, 32, v18
	v_or_b32_e32 v178, 48, v18
	v_lshlrev_b64 v[18:19], 11, v[18:19]
	v_ashrrev_i32_e32 v23, 31, v22
	v_lshl_add_u64 v[18:19], s[18:19], 0, v[18:19]
	v_lshlrev_b64 v[22:23], 11, v[22:23]
	v_lshl_add_u64 v[18:19], v[18:19], 0, v[20:21]
	v_lshl_add_u64 v[22:23], s[18:19], 0, v[22:23]
	v_lshl_add_u64 v[180:181], v[22:23], 0, v[20:21]
	v_mov_b32_e32 v32, 0
	v_mov_b32_e32 v33, 0
	v_ashrrev_i32_e32 v177, 31, v176
	v_ashrrev_i32_e32 v179, 31, v178
	v_lshlrev_b64 v[176:177], 11, v[176:177]
	v_lshlrev_b64 v[178:179], 11, v[178:179]
	v_lshl_add_u64 v[176:177], s[18:19], 0, v[176:177]
	v_lshl_add_u64 v[178:179], s[18:19], 0, v[178:179]
	v_lshl_add_u64 v[176:177], v[176:177], 0, v[20:21]
	v_lshl_add_u64 v[178:179], v[178:179], 0, v[20:21]
	v_lshl_add_u64 v[188:189], v[18:19], 0, s[14:15]
	v_lshl_add_u64 v[190:191], v[18:19], 0, s[24:25]
	v_lshl_add_u64 v[22:23], v[18:19], 0, s[26:27]
	v_lshl_add_u64 v[20:21], v[18:19], 0, s[28:29]
	s_nop 0
	v_pk_fma_f32 v[158:159], v[158:159], s[30:31], v[14:15] op_sel_hi:[1,0,1]
	v_pk_fma_f32 v[154:155], v[154:155], s[30:31], v[10:11] op_sel_hi:[1,0,1]
	v_pk_fma_f32 v[138:139], v[138:139], s[30:31], v[6:7] op_sel_hi:[1,0,1]
	v_pk_fma_f32 v[130:131], v[130:131], s[30:31], v[2:3] op_sel_hi:[1,0,1]
	v_cvt_pk_fp8_f32 v24, v158, v159
	v_cvt_pk_fp8_f32 v25, v154, v155
	v_pk_fma_f32 v[150:151], v[150:151], s[30:31], v[14:15] op_sel_hi:[1,0,1]
	v_pk_fma_f32 v[146:147], v[146:147], s[30:31], v[10:11] op_sel_hi:[1,0,1]
	v_cvt_pk_fp8_f32 v26, v138, v139
	v_cvt_pk_fp8_f32 v27, v130, v131
	v_pk_fma_f32 v[126:127], v[126:127], s[30:31], v[6:7] op_sel_hi:[1,0,1]
	v_pk_fma_f32 v[122:123], v[122:123], s[30:31], v[2:3] op_sel_hi:[1,0,1]
	v_cvt_pk_fp8_f32 v28, v150, v151
	v_cvt_pk_fp8_f32 v29, v146, v147
	v_pk_fma_f32 v[160:161], v[160:161], s[30:31], v[16:17] op_sel_hi:[1,0,1]
	v_pk_fma_f32 v[156:157], v[156:157], s[30:31], v[12:13] op_sel_hi:[1,0,1]
	v_cvt_pk_fp8_f32 v30, v126, v127
	v_cvt_pk_fp8_f32 v31, v122, v123
	v_pk_fma_f32 v[140:141], v[140:141], s[30:31], v[8:9] op_sel_hi:[1,0,1]
	v_pk_fma_f32 v[132:133], v[132:133], s[30:31], v[4:5] op_sel_hi:[1,0,1]
	v_pk_fma_f32 v[114:115], v[114:115], s[30:31], v[6:7] op_sel_hi:[1,0,1]
	v_pk_fma_f32 v[106:107], v[106:107], s[30:31], v[2:3] op_sel_hi:[1,0,1]
	v_cvt_pk_fp8_f32 v24, v160, v161 op_sel:[0,0,1]
	v_cvt_pk_fp8_f32 v25, v156, v157 op_sel:[0,0,1]
	v_pk_fma_f32 v[152:153], v[152:153], s[30:31], v[16:17] op_sel_hi:[1,0,1]
	v_pk_fma_f32 v[148:149], v[148:149], s[30:31], v[12:13] op_sel_hi:[1,0,1]
	v_cvt_pk_fp8_f32 v174, v114, v115
	v_cvt_pk_fp8_f32 v26, v140, v141 op_sel:[0,0,1]
	v_cvt_pk_fp8_f32 v27, v132, v133 op_sel:[0,0,1]
	v_cvt_pk_fp8_f32 v175, v106, v107
	v_pk_fma_f32 v[128:129], v[128:129], s[30:31], v[8:9] op_sel_hi:[1,0,1]
	v_pk_fma_f32 v[124:125], v[124:125], s[30:31], v[4:5] op_sel_hi:[1,0,1]
	v_cvt_pk_fp8_f32 v28, v152, v153 op_sel:[0,0,1]
	v_cvt_pk_fp8_f32 v29, v148, v149 op_sel:[0,0,1]
	v_cvt_pk_fp8_f32 v30, v128, v129 op_sel:[0,0,1]
	v_cvt_pk_fp8_f32 v31, v124, v125 op_sel:[0,0,1]
	v_mov_b32_e32 v222, v24
	v_mov_b32_e32 v223, v25
	v_mov_b32_e32 v224, v26
	v_mov_b32_e32 v225, v27
	s_nop 1
	v_permlane16_swap_b32 v222, v224
	v_permlane16_swap_b32 v223, v225
	v_mov_b32_e32 v226, v28
	v_mov_b32_e32 v227, v29
	v_mov_b32_e32 v228, v30
	v_mov_b32_e32 v229, v31
	s_nop 1
	v_permlane16_swap_b32 v226, v228
	v_permlane16_swap_b32 v227, v229
	v_pk_fma_f32 v[24:25], v[116:117], s[30:31], v[8:9] op_sel_hi:[1,0,1]
	v_pk_fma_f32 v[26:27], v[108:109], s[30:31], v[4:5] op_sel_hi:[1,0,1]
	v_cvt_pk_fp8_f32 v174, v24, v25 op_sel:[0,0,1]
	v_cvt_pk_fp8_f32 v175, v26, v27 op_sel:[0,0,1]
	v_pk_fma_f32 v[24:25], v[118:119], s[30:31], v[14:15] op_sel_hi:[1,0,1]
	v_pk_fma_f32 v[26:27], v[110:111], s[30:31], v[10:11] op_sel_hi:[1,0,1]
	v_mov_b32_e32 v28, 0
	v_mov_b32_e32 v29, 0
	v_cvt_pk_fp8_f32 v28, v24, v25
	v_cvt_pk_fp8_f32 v29, v26, v27
	v_pk_fma_f32 v[142:143], v[142:143], s[30:31], v[14:15] op_sel_hi:[1,0,1]
	v_pk_fma_f32 v[134:135], v[134:135], s[30:31], v[10:11] op_sel_hi:[1,0,1]
	v_cvt_pk_fp8_f32 v32, v142, v143
	v_cvt_pk_fp8_f32 v33, v134, v135
	v_pk_fma_f32 v[24:25], v[120:121], s[30:31], v[16:17] op_sel_hi:[1,0,1]
	v_pk_fma_f32 v[26:27], v[112:113], s[30:31], v[12:13] op_sel_hi:[1,0,1]
	v_cvt_pk_fp8_f32 v28, v24, v25 op_sel:[0,0,1]
	v_cvt_pk_fp8_f32 v29, v26, v27 op_sel:[0,0,1]
	v_pk_fma_f32 v[24:25], v[102:103], s[30:31], v[6:7] op_sel_hi:[1,0,1]
	v_pk_fma_f32 v[26:27], v[98:99], s[30:31], v[2:3] op_sel_hi:[1,0,1]
	v_mov_b32_e32 v30, 0
	v_mov_b32_e32 v31, 0
	v_pk_fma_f32 v[144:145], v[144:145], s[30:31], v[16:17] op_sel_hi:[1,0,1]
	v_pk_fma_f32 v[136:137], v[136:137], s[30:31], v[12:13] op_sel_hi:[1,0,1]
	v_cvt_pk_fp8_f32 v30, v24, v25
	v_cvt_pk_fp8_f32 v31, v26, v27
	v_cvt_pk_fp8_f32 v32, v144, v145 op_sel:[0,0,1]
	v_cvt_pk_fp8_f32 v33, v136, v137 op_sel:[0,0,1]
	v_pk_fma_f32 v[24:25], v[104:105], s[30:31], v[8:9] op_sel_hi:[1,0,1]
	v_pk_fma_f32 v[26:27], v[100:101], s[30:31], v[4:5] op_sel_hi:[1,0,1]
	v_cvt_pk_fp8_f32 v30, v24, v25 op_sel:[0,0,1]
	v_cvt_pk_fp8_f32 v31, v26, v27 op_sel:[0,0,1]
	v_mov_b32_e32 v230, v32
	v_mov_b32_e32 v231, v33
	v_mov_b32_e32 v232, v174
	v_mov_b32_e32 v233, v175
	s_nop 1
	v_permlane16_swap_b32 v230, v232
	v_permlane16_swap_b32 v231, v233
	v_mov_b32_e32 v234, v28
	s_and_b64 vcc, exec, s[22:23]
	s_cbranch_vccz .Lp10_lbar
	s_barrier
.Lp10_lbar:
	v_mov_b32_e32 v235, v29
	v_mov_b32_e32 v236, v30
	v_mov_b32_e32 v237, v31
	s_nop 1
	v_permlane16_swap_b32 v234, v236
	v_permlane16_swap_b32 v235, v237
	v_pk_fma_f32 v[24:25], v[94:95], s[30:31], v[14:15] op_sel_hi:[1,0,1]
	v_pk_fma_f32 v[26:27], v[90:91], s[30:31], v[10:11] op_sel_hi:[1,0,1]
	v_mov_b32_e32 v28, 0
	v_mov_b32_e32 v29, 0
	v_cvt_pk_fp8_f32 v28, v24, v25
	v_cvt_pk_fp8_f32 v29, v26, v27
	v_pk_fma_f32 v[24:25], v[96:97], s[30:31], v[16:17] op_sel_hi:[1,0,1]
	v_pk_fma_f32 v[26:27], v[92:93], s[30:31], v[12:13] op_sel_hi:[1,0,1]
	v_cvt_pk_fp8_f32 v28, v24, v25 op_sel:[0,0,1]
	v_cvt_pk_fp8_f32 v29, v26, v27 op_sel:[0,0,1]
	v_pk_fma_f32 v[24:25], v[82:83], s[30:31], v[6:7] op_sel_hi:[1,0,1]
	v_pk_fma_f32 v[26:27], v[70:71], s[30:31], v[2:3] op_sel_hi:[1,0,1]
	v_mov_b32_e32 v30, 0
	v_mov_b32_e32 v31, 0
	v_cvt_pk_fp8_f32 v30, v24, v25
	v_cvt_pk_fp8_f32 v31, v26, v27
	v_pk_fma_f32 v[24:25], v[84:85], s[30:31], v[8:9] op_sel_hi:[1,0,1]
	v_pk_fma_f32 v[26:27], v[72:73], s[30:31], v[4:5] op_sel_hi:[1,0,1]
	v_cvt_pk_fp8_f32 v30, v24, v25 op_sel:[0,0,1]
	v_cvt_pk_fp8_f32 v31, v26, v27 op_sel:[0,0,1]
	v_add_co_u32_e32 v24, vcc, s58, v18
	v_pk_fma_f32 v[26:27], v[66:67], s[30:31], v[10:11] op_sel_hi:[1,0,1]
	s_nop 0
	v_addc_co_u32_e32 v25, vcc, 0, v19, vcc
	v_mov_b32_e32 v238, v28
	v_mov_b32_e32 v239, v29
	v_mov_b32_e32 v240, v30
	v_mov_b32_e32 v241, v31
	s_nop 1
	v_permlane16_swap_b32 v238, v240
	v_permlane16_swap_b32 v239, v241
	v_pk_fma_f32 v[24:25], v[78:79], s[30:31], v[14:15] op_sel_hi:[1,0,1]
	v_mov_b32_e32 v28, 0
	v_mov_b32_e32 v29, 0
	v_cvt_pk_fp8_f32 v28, v24, v25
	v_cvt_pk_fp8_f32 v29, v26, v27
	v_pk_fma_f32 v[24:25], v[80:81], s[30:31], v[16:17] op_sel_hi:[1,0,1]
	v_pk_fma_f32 v[26:27], v[68:69], s[30:31], v[12:13] op_sel_hi:[1,0,1]
	v_cvt_pk_fp8_f32 v28, v24, v25 op_sel:[0,0,1]
	v_cvt_pk_fp8_f32 v29, v26, v27 op_sel:[0,0,1]
	v_pk_fma_f32 v[24:25], v[54:55], s[30:31], v[6:7] op_sel_hi:[1,0,1]
	v_pk_fma_f32 v[26:27], v[42:43], s[30:31], v[2:3] op_sel_hi:[1,0,1]
	v_mov_b32_e32 v30, 0
	v_mov_b32_e32 v31, 0
	v_cvt_pk_fp8_f32 v30, v24, v25
	v_cvt_pk_fp8_f32 v31, v26, v27
	v_pk_fma_f32 v[24:25], v[56:57], s[30:31], v[8:9] op_sel_hi:[1,0,1]
	v_pk_fma_f32 v[26:27], v[44:45], s[30:31], v[4:5] op_sel_hi:[1,0,1]
	v_cvt_pk_fp8_f32 v30, v24, v25 op_sel:[0,0,1]
	v_cvt_pk_fp8_f32 v31, v26, v27 op_sel:[0,0,1]
	v_add_co_u32_e32 v24, vcc, s82, v18
	v_pk_fma_f32 v[26:27], v[46:47], s[30:31], v[10:11] op_sel_hi:[1,0,1]
	s_nop 0
	v_addc_co_u32_e32 v25, vcc, 0, v19, vcc
	v_mov_b32_e32 v242, v28
	v_mov_b32_e32 v243, v29
	v_mov_b32_e32 v244, v30
	v_mov_b32_e32 v245, v31
	s_nop 1
	v_permlane16_swap_b32 v242, v244
	v_permlane16_swap_b32 v243, v245
	v_pk_fma_f32 v[24:25], v[50:51], s[30:31], v[14:15] op_sel_hi:[1,0,1]
	v_mov_b32_e32 v28, 0
	v_mov_b32_e32 v29, 0
	v_cvt_pk_fp8_f32 v28, v24, v25
	v_cvt_pk_fp8_f32 v29, v26, v27
	v_pk_fma_f32 v[24:25], v[52:53], s[30:31], v[16:17] op_sel_hi:[1,0,1]
	v_pk_fma_f32 v[26:27], v[48:49], s[30:31], v[12:13] op_sel_hi:[1,0,1]
	v_cvt_pk_fp8_f32 v28, v24, v25 op_sel:[0,0,1]
	v_cvt_pk_fp8_f32 v29, v26, v27 op_sel:[0,0,1]
	v_pk_fma_f32 v[24:25], v[74:75], s[30:31], v[6:7] op_sel_hi:[1,0,1]
	v_pk_fma_f32 v[26:27], v[86:87], s[30:31], v[2:3] op_sel_hi:[1,0,1]
	v_mov_b32_e32 v30, 0
	v_mov_b32_e32 v31, 0
	v_cvt_pk_fp8_f32 v30, v24, v25
	v_cvt_pk_fp8_f32 v31, v26, v27
	v_pk_fma_f32 v[24:25], v[76:77], s[30:31], v[8:9] op_sel_hi:[1,0,1]
	v_pk_fma_f32 v[26:27], v[88:89], s[30:31], v[4:5] op_sel_hi:[1,0,1]
	v_cvt_pk_fp8_f32 v30, v24, v25 op_sel:[0,0,1]
	v_cvt_pk_fp8_f32 v31, v26, v27 op_sel:[0,0,1]
	v_add_co_u32_e32 v24, vcc, s83, v18
	v_pk_fma_f32 v[14:15], v[38:39], s[30:31], v[14:15] op_sel_hi:[1,0,1]
	s_nop 0
	v_addc_co_u32_e32 v25, vcc, 0, v19, vcc
	v_mov_b32_e32 v246, v28
	v_mov_b32_e32 v247, v29
	v_mov_b32_e32 v248, v30
	v_mov_b32_e32 v249, v31
	s_nop 1
	v_permlane16_swap_b32 v246, v248
	v_permlane16_swap_b32 v247, v249
	v_mov_b32_e32 v22, 0
	v_cvt_pk_fp8_f32 v22, v14, v15
	v_pk_fma_f32 v[10:11], v[34:35], s[30:31], v[10:11] op_sel_hi:[1,0,1]
	v_mov_b32_e32 v23, 0
	v_cvt_pk_fp8_f32 v23, v10, v11
	v_pk_fma_f32 v[10:11], v[40:41], s[30:31], v[16:17] op_sel_hi:[1,0,1]
	v_pk_fma_f32 v[6:7], v[58:59], s[30:31], v[6:7] op_sel_hi:[1,0,1]
	v_cvt_pk_fp8_f32 v22, v10, v11 op_sel:[0,0,1]
	v_pk_fma_f32 v[2:3], v[62:63], s[30:31], v[2:3] op_sel_hi:[1,0,1]
	v_mov_b32_e32 v10, 0
	v_mov_b32_e32 v11, 0
	v_cvt_pk_fp8_f32 v10, v6, v7
	v_cvt_pk_fp8_f32 v11, v2, v3
	v_pk_fma_f32 v[12:13], v[36:37], s[30:31], v[12:13] op_sel_hi:[1,0,1]
	v_pk_fma_f32 v[2:3], v[60:61], s[30:31], v[8:9] op_sel_hi:[1,0,1]
	v_cvt_pk_fp8_f32 v23, v12, v13 op_sel:[0,0,1]
	v_pk_fma_f32 v[4:5], v[64:65], s[30:31], v[4:5] op_sel_hi:[1,0,1]
	v_cvt_pk_fp8_f32 v10, v2, v3 op_sel:[0,0,1]
	v_cvt_pk_fp8_f32 v11, v4, v5 op_sel:[0,0,1]
	v_add_co_u32_e32 v2, vcc, s84, v18
	s_nop 1
	v_addc_co_u32_e32 v3, vcc, 0, v19, vcc
	s_andn2_b64 vcc, exec, s[6:7]
	s_mov_b64 s[6:7], -1
	v_mov_b32_e32 v250, v22
	v_mov_b32_e32 v251, v23
	v_mov_b32_e32 v252, v10
	v_mov_b32_e32 v253, v11
	s_nop 1
	v_permlane16_swap_b32 v250, v252
	v_permlane16_swap_b32 v251, v253
	s_cbranch_vccnz .LBB0_1434
	s_andn2_b64 vcc, exec, s[16:17]
	s_cbranch_vccnz .LBB0_1433
	s_barrier
	s_branch .LBB0_1433
